# v63 + work-queue tail split from entry 16: entries 16..63 keep half of their weight-copy chunk, 48 extra copy-only entries per XCD (112 entries)
# baseline (speedup 1.0000x reference)
.LBB6_896:
	s_or_b64 exec, exec, s[2:3]
	v_readlane_b32 s0, v254, 30
	s_waitcnt lgkmcnt(0)
	s_barrier
	v_mov_b32_e32 v2, s0
	ds_read_b32 v2, v2
	s_mov_b64 s[2:3], -1
	s_waitcnt lgkmcnt(0)
	s_barrier
	v_readfirstlane_b32 s0, v2
	s_cmp_gt_i32 s0, 0x6f
	s_cbranch_scc1 .LBB6_891
	s_cmp_gt_i32 s0, 47
	s_cbranch_scc0 .LBB6_899
	s_sub_i32 s1, s0, 48
	s_lshr_b32 s92, s1, 1
	s_mov_b64 s[2:3], 0

.LBB6_901:
	s_lshl_b32 s84, s0, 3
	s_or_b32 s1, s84, s59
	s_lshl_b32 s2, s1, 1
	s_add_i32 s3, s1, 0x80
	s_cmp_lt_u32 s1, 0x80
	s_cselect_b32 s2, s2, s3
	s_mul_i32 s2, s63, s2
	s_lshr_b32 s2, s2, 10
	s_and_b32 s90, s2, 0xffffffe0
	s_add_i32 s1, s1, 1
	s_lshl_b32 s2, s1, 1
	s_add_i32 s3, s1, 0x80
	s_cmp_lt_u32 s1, 0x80
	s_cselect_b32 s2, s2, s3
	s_mul_i32 s2, s63, s2
	s_lshr_b32 s2, s2, 10
	s_and_b32 s91, s2, 0xffffffe0
	s_bitcmp0_b32 s0, 0
	s_cselect_b64 s[22:23], -1, 0
	s_and_b64 vcc, exec, s[22:23]
	s_cbranch_vccnz .LBB6_1210
	v_readfirstlane_b32 s98, v0
	s_nop 0
	s_bitcmp1_b32 s98, 8
	s_cbranch_scc0 .Ldephase_a
	s_sleep 80
